# expert tables built once: P7/P8 tables derived in LDS, P9 reuses P8 table (on top of v2)
# speedup vs baseline: 1.0030x; 1.0030x over previous
.LBB0_740:
	s_waitcnt lgkmcnt(0)
	s_barrier
	s_and_saveexec_b64 s[2:3], s[66:67]
	s_cbranch_execz .LBB0_742
	v_mov_b32_e32 v0, 0x20a40
	ds_read_b128 v[4:7], v0
	ds_read_b128 v[8:11], v0 offset:16
	ds_read_b128 v[12:15], v0 offset:32
	ds_read_b128 v[16:19], v0 offset:48
	ds_read_b128 v[20:23], v0 offset:64
	ds_read_b128 v[24:27], v0 offset:80
	ds_read_b128 v[28:31], v0 offset:96
	ds_read_b128 v[64:67], v0 offset:112
	ds_read_b32 v68, v0 offset:128
	s_waitcnt lgkmcnt(0)
	v_lshlrev_b32_e32 v4, 1, v4
	v_lshlrev_b32_e32 v5, 1, v5
	v_lshlrev_b32_e32 v6, 1, v6
	v_lshlrev_b32_e32 v7, 1, v7
	v_lshlrev_b32_e32 v8, 1, v8
	v_lshlrev_b32_e32 v9, 1, v9
	v_lshlrev_b32_e32 v10, 1, v10
	v_lshlrev_b32_e32 v11, 1, v11
	v_lshlrev_b32_e32 v12, 1, v12
	v_lshlrev_b32_e32 v13, 1, v13
	v_lshlrev_b32_e32 v14, 1, v14
	v_lshlrev_b32_e32 v15, 1, v15
	v_lshlrev_b32_e32 v16, 1, v16
	v_lshlrev_b32_e32 v17, 1, v17
	v_lshlrev_b32_e32 v18, 1, v18
	v_lshlrev_b32_e32 v19, 1, v19
	v_lshlrev_b32_e32 v20, 1, v20
	v_lshlrev_b32_e32 v21, 1, v21
	v_lshlrev_b32_e32 v22, 1, v22
	v_lshlrev_b32_e32 v23, 1, v23
	v_lshlrev_b32_e32 v24, 1, v24
	v_lshlrev_b32_e32 v25, 1, v25
	v_lshlrev_b32_e32 v26, 1, v26
	v_lshlrev_b32_e32 v27, 1, v27
	v_lshlrev_b32_e32 v28, 1, v28
	v_lshlrev_b32_e32 v29, 1, v29
	v_lshlrev_b32_e32 v30, 1, v30
	v_lshlrev_b32_e32 v31, 1, v31
	v_lshlrev_b32_e32 v64, 1, v64
	v_lshlrev_b32_e32 v65, 1, v65
	v_lshlrev_b32_e32 v66, 1, v66
	v_lshlrev_b32_e32 v67, 1, v67
	v_lshlrev_b32_e32 v68, 1, v68
	ds_write_b128 v0, v[4:7]
	ds_write_b128 v0, v[8:11] offset:16
	ds_write_b128 v0, v[12:15] offset:32
	ds_write_b128 v0, v[16:19] offset:48
	ds_write_b128 v0, v[20:23] offset:64
	ds_write_b128 v0, v[24:27] offset:80
	ds_write_b128 v0, v[28:31] offset:96
	ds_write_b128 v0, v[64:67] offset:112
	ds_write_b32 v0, v68 offset:128

.LBB0_939:
	s_andn2_b64 vcc, exec, s[0:1]
	s_cbranch_vccnz .LBB0_1052
	s_waitcnt lgkmcnt(0)
	s_barrier
	s_and_saveexec_b64 s[2:3], s[66:67]
	s_cbranch_execz .LBB0_942
	v_mov_b32_e32 v0, 0x20a40
	ds_read_b128 v[4:7], v0
	ds_read_b128 v[8:11], v0 offset:16
	ds_read_b128 v[12:15], v0 offset:32
	ds_read_b128 v[16:19], v0 offset:48
	ds_read_b128 v[20:23], v0 offset:64
	ds_read_b128 v[24:27], v0 offset:80
	ds_read_b128 v[28:31], v0 offset:96
	ds_read_b128 v[64:67], v0 offset:112
	ds_read_b32 v68, v0 offset:128
	s_waitcnt lgkmcnt(0)
	v_lshrrev_b32_e32 v4, 1, v4
	v_lshrrev_b32_e32 v5, 1, v5
	v_lshrrev_b32_e32 v6, 1, v6
	v_lshrrev_b32_e32 v7, 1, v7
	v_lshrrev_b32_e32 v8, 1, v8
	v_lshrrev_b32_e32 v9, 1, v9
	v_lshrrev_b32_e32 v10, 1, v10
	v_lshrrev_b32_e32 v11, 1, v11
	v_lshrrev_b32_e32 v12, 1, v12
	v_lshrrev_b32_e32 v13, 1, v13
	v_lshrrev_b32_e32 v14, 1, v14
	v_lshrrev_b32_e32 v15, 1, v15
	v_lshrrev_b32_e32 v16, 1, v16
	v_lshrrev_b32_e32 v17, 1, v17
	v_lshrrev_b32_e32 v18, 1, v18
	v_lshrrev_b32_e32 v19, 1, v19
	v_lshrrev_b32_e32 v20, 1, v20
	v_lshrrev_b32_e32 v21, 1, v21
	v_lshrrev_b32_e32 v22, 1, v22
	v_lshrrev_b32_e32 v23, 1, v23
	v_lshrrev_b32_e32 v24, 1, v24
	v_lshrrev_b32_e32 v25, 1, v25
	v_lshrrev_b32_e32 v26, 1, v26
	v_lshrrev_b32_e32 v27, 1, v27
	v_lshrrev_b32_e32 v28, 1, v28
	v_lshrrev_b32_e32 v29, 1, v29
	v_lshrrev_b32_e32 v30, 1, v30
	v_lshrrev_b32_e32 v31, 1, v31
	v_lshrrev_b32_e32 v64, 1, v64
	v_lshrrev_b32_e32 v65, 1, v65
	v_lshrrev_b32_e32 v66, 1, v66
	v_lshrrev_b32_e32 v67, 1, v67
	v_lshrrev_b32_e32 v68, 1, v68
	ds_write_b128 v0, v[4:7]
	ds_write_b128 v0, v[8:11] offset:16
	ds_write_b128 v0, v[12:15] offset:32
	ds_write_b128 v0, v[16:19] offset:48
	ds_write_b128 v0, v[20:23] offset:64
	ds_write_b128 v0, v[24:27] offset:80
	ds_write_b128 v0, v[28:31] offset:96
	ds_write_b128 v0, v[64:67] offset:112
	ds_write_b32 v0, v68 offset:128

.LBB0_1089:
	s_cmp_lt_i32 s94, 10
	s_cselect_b64 s[0:1], -1, 0
	s_and_b64 s[0:1], s[0:1], s[2:3]
	s_andn2_b64 vcc, exec, s[0:1]
	s_cbranch_vccnz .LBB0_1095
	s_waitcnt lgkmcnt(0)
	s_barrier
	s_and_saveexec_b64 s[0:1], s[66:67]
.LBB0_1092:
	s_or_b64 exec, exec, s[0:1]
	s_waitcnt vmcnt(0)
	v_lshl_add_u32 v12, s33, 3, v179
	s_movk_i32 s0, 0x2000
	v_cmp_gt_i32_e32 vcc, s0, v12
	s_waitcnt lgkmcnt(0)
	s_barrier
	s_and_saveexec_b64 s[0:1], vcc
	s_cbranch_execz .LBB0_1095
	v_lshlrev_b32_e32 v0, 3, v178
	v_and_b32_e32 v14, 0x1f8, v0
	v_mov_b32_e32 v15, 0
	v_lshl_add_u64 v[0:1], s[90:91], 0, v[14:15]
	s_mov_b64 s[6:7], 0x191a0000
	v_ashrrev_i32_e32 v13, 31, v12
	s_add_u32 s0, s90, 0xf040000
	v_lshl_add_u64 v[16:17], v[0:1], 0, s[6:7]
	v_lshlrev_b64 v[0:1], 12, v[12:13]
	v_and_b32_e32 v2, 63, v178
	s_addc_u32 s1, s91, 0
	v_lshl_or_b32 v0, v2, 4, v0
	s_add_u32 s2, s90, 0xf060000
	v_lshl_add_u64 v[0:1], s[90:91], 0, v[0:1]
	s_mov_b64 s[8:9], 0x9040000
	s_addc_u32 s3, s91, 0
	v_lshl_add_u64 v[18:19], v[0:1], 0, s[8:9]
	v_lshlrev_b32_e32 v0, 2, v179
	s_add_u32 s4, s90, 0xf080000
	v_lshl_add_u32 v20, s33, 5, v0
	v_lshlrev_b64 v[0:1], 13, v[12:13]
	s_addc_u32 s5, s91, 0
	s_lshl_b32 s6, s96, 3
	v_lshl_or_b32 v0, v2, 5, v0
	s_ashr_i32 s7, s6, 31
	v_lshl_add_u64 v[0:1], s[88:89], 0, v[0:1]
	s_mov_b64 s[10:11], 0x1000
	s_lshl_b64 s[8:9], s[6:7], 12
	v_lshl_add_u64 v[22:23], v[0:1], 0, s[10:11]
	s_lshl_b64 s[10:11], s[6:7], 13
	s_mov_b32 s7, 0x20840
	s_lshl_b32 s20, s96, 5
	s_mov_b64 s[12:13], 0
	s_addk_i32 s7, 0x100
	v_lshlrev_b32_e32 v14, 2, v14
	s_mov_b64 s[14:15], 0xa000
	s_mov_b64 s[16:17], 0xb000
	s_mov_b32 s21, 0xb000
	s_mov_b64 s[18:19], 0xb800
	s_movk_i32 s22, 0x1fff
